# MFMA/LDS interleave (strategy 8) in ml_kvloc: the 34-MFMA section software-pipelined by hand, B fragments through a 4-slot register ring three MFMAs ahead, counted lgkmcnt; on top of v54
# speedup vs baseline: 1.0231x; 1.0007x over previous
.LBB0_408:
	s_waitcnt lgkmcnt(0)
	s_barrier
	ds_read_b64_tr_b16 v[102:103], v141 offset:2048
	ds_read_b64_tr_b16 v[104:105], v141 offset:3136
	ds_read_b64_tr_b16 v[186:187], v141 offset:10752
	ds_read_b64_tr_b16 v[188:189], v141 offset:11840
	ds_read_b64_tr_b16 v[170:171], v123 offset:19456
	ds_read_b64_tr_b16 v[172:173], v123 offset:21696
	ds_read_b64_tr_b16 v[174:175], v123 offset:19488
	ds_read_b64_tr_b16 v[176:177], v123 offset:21728
	ds_read_b64_tr_b16 v[178:179], v123 offset:19520
	ds_read_b64_tr_b16 v[180:181], v123 offset:21760
	ds_read_b64_tr_b16 v[182:183], v123 offset:19552
	ds_read_b64_tr_b16 v[184:185], v123 offset:21792
	s_waitcnt lgkmcnt(6)
	v_mfma_f32_16x16x32_bf16 v[98:101], v[102:105], v[170:173], v[98:101]
	ds_read_b64_tr_b16 v[170:171], v123 offset:19584
	ds_read_b64_tr_b16 v[172:173], v123 offset:21824
	s_waitcnt lgkmcnt(6)
	v_mfma_f32_16x16x32_bf16 v[94:97], v[102:105], v[174:177], v[94:97]
	ds_read_b64_tr_b16 v[174:175], v123 offset:19616
	ds_read_b64_tr_b16 v[176:177], v123 offset:21856
	s_waitcnt lgkmcnt(6)
	v_mfma_f32_16x16x32_bf16 v[90:93], v[102:105], v[178:181], v[90:93]
	ds_read_b64_tr_b16 v[178:179], v123 offset:19648
	ds_read_b64_tr_b16 v[180:181], v123 offset:21888
	s_waitcnt lgkmcnt(6)
	v_mfma_f32_16x16x32_bf16 v[86:89], v[102:105], v[182:185], v[86:89]
	ds_read_b64_tr_b16 v[182:183], v123 offset:19680
	ds_read_b64_tr_b16 v[184:185], v123 offset:21920
	s_waitcnt lgkmcnt(6)
	v_mfma_f32_16x16x32_bf16 v[82:85], v[102:105], v[170:173], v[82:85]
	ds_read_b64_tr_b16 v[170:171], v123 offset:19712
	ds_read_b64_tr_b16 v[172:173], v123 offset:21952
	s_waitcnt lgkmcnt(6)
	v_mfma_f32_16x16x32_bf16 v[78:81], v[102:105], v[174:177], v[78:81]
	ds_read_b64_tr_b16 v[174:175], v123 offset:19744
	ds_read_b64_tr_b16 v[176:177], v123 offset:21984
	s_waitcnt lgkmcnt(6)
	v_mfma_f32_16x16x32_bf16 v[74:77], v[102:105], v[178:181], v[74:77]
	ds_read_b64_tr_b16 v[178:179], v123 offset:19776
	ds_read_b64_tr_b16 v[180:181], v123 offset:22016
	s_waitcnt lgkmcnt(6)
	v_mfma_f32_16x16x32_bf16 v[70:73], v[102:105], v[182:185], v[70:73]
	ds_read_b64_tr_b16 v[182:183], v123 offset:19808
	ds_read_b64_tr_b16 v[184:185], v123 offset:22048
	s_waitcnt lgkmcnt(6)
	v_mfma_f32_16x16x32_bf16 v[66:69], v[102:105], v[170:173], v[66:69]
	ds_read_b64_tr_b16 v[170:171], v123 offset:19840
	ds_read_b64_tr_b16 v[172:173], v123 offset:22080
	s_waitcnt lgkmcnt(6)
	v_mfma_f32_16x16x32_bf16 v[62:65], v[102:105], v[174:177], v[62:65]
	ds_read_b64_tr_b16 v[174:175], v123 offset:19872
	ds_read_b64_tr_b16 v[176:177], v123 offset:22112
	s_waitcnt lgkmcnt(6)
	v_mfma_f32_16x16x32_bf16 v[58:61], v[102:105], v[178:181], v[58:61]
	ds_read_b64_tr_b16 v[178:179], v123 offset:19904
	ds_read_b64_tr_b16 v[180:181], v123 offset:22144
	s_waitcnt lgkmcnt(6)
	v_mfma_f32_16x16x32_bf16 v[54:57], v[102:105], v[182:185], v[54:57]
	ds_read_b64_tr_b16 v[182:183], v123 offset:19936
	ds_read_b64_tr_b16 v[184:185], v123 offset:22176
	s_waitcnt lgkmcnt(6)
	v_mfma_f32_16x16x32_bf16 v[46:49], v[102:105], v[170:173], v[46:49]
	ds_read_b64_tr_b16 v[170:171], v123 offset:19968
	ds_read_b64_tr_b16 v[172:173], v123 offset:22208
	s_waitcnt lgkmcnt(6)
	v_mfma_f32_16x16x32_bf16 v[42:45], v[102:105], v[174:177], v[42:45]
	ds_read_b64_tr_b16 v[174:175], v123 offset:37376
	ds_read_b64_tr_b16 v[176:177], v123 offset:39616
	s_waitcnt lgkmcnt(6)
	v_mfma_f32_16x16x32_bf16 v[38:41], v[102:105], v[178:181], v[38:41]
	ds_read_b64_tr_b16 v[178:179], v123 offset:37408
	ds_read_b64_tr_b16 v[180:181], v123 offset:39648
	s_waitcnt lgkmcnt(6)
	v_mfma_f32_16x16x32_bf16 v[34:37], v[102:105], v[182:185], v[34:37]
	ds_read_b64_tr_b16 v[182:183], v123 offset:37440
	ds_read_b64_tr_b16 v[184:185], v123 offset:39680
	s_waitcnt lgkmcnt(6)
	v_mfma_f32_16x16x32_bf16 v[50:53], v[102:105], v[170:173], v[50:53]
	ds_read_b64_tr_b16 v[170:171], v123 offset:37472
	ds_read_b64_tr_b16 v[172:173], v123 offset:39712
	s_waitcnt lgkmcnt(6)
	v_mfma_f32_16x16x32_bf16 v[98:101], v[186:189], v[174:177], v[98:101]
	ds_read_b64_tr_b16 v[174:175], v123 offset:37504
	ds_read_b64_tr_b16 v[176:177], v123 offset:39744
	s_waitcnt lgkmcnt(6)
	v_mfma_f32_16x16x32_bf16 v[94:97], v[186:189], v[178:181], v[94:97]
	ds_read_b64_tr_b16 v[178:179], v123 offset:37536
	ds_read_b64_tr_b16 v[180:181], v123 offset:39776
	s_waitcnt lgkmcnt(6)
	v_mfma_f32_16x16x32_bf16 v[90:93], v[186:189], v[182:185], v[90:93]
	ds_read_b64_tr_b16 v[182:183], v123 offset:37568
	ds_read_b64_tr_b16 v[184:185], v123 offset:39808
	s_waitcnt lgkmcnt(6)
	v_mfma_f32_16x16x32_bf16 v[86:89], v[186:189], v[170:173], v[86:89]
	ds_read_b64_tr_b16 v[170:171], v123 offset:37600
	ds_read_b64_tr_b16 v[172:173], v123 offset:39840
	s_waitcnt lgkmcnt(6)
	v_mfma_f32_16x16x32_bf16 v[82:85], v[186:189], v[174:177], v[82:85]
	ds_read_b64_tr_b16 v[174:175], v123 offset:37632
	ds_read_b64_tr_b16 v[176:177], v123 offset:39872
	s_waitcnt lgkmcnt(6)
	v_mfma_f32_16x16x32_bf16 v[78:81], v[186:189], v[178:181], v[78:81]
	ds_read_b64_tr_b16 v[178:179], v123 offset:37664
	ds_read_b64_tr_b16 v[180:181], v123 offset:39904
	s_waitcnt lgkmcnt(6)
	v_mfma_f32_16x16x32_bf16 v[74:77], v[186:189], v[182:185], v[74:77]
	ds_read_b64_tr_b16 v[182:183], v123 offset:37696
	ds_read_b64_tr_b16 v[184:185], v123 offset:39936
	s_waitcnt lgkmcnt(6)
	v_mfma_f32_16x16x32_bf16 v[70:73], v[186:189], v[170:173], v[70:73]
	ds_read_b64_tr_b16 v[170:171], v123 offset:37728
	ds_read_b64_tr_b16 v[172:173], v123 offset:39968
	s_waitcnt lgkmcnt(6)
	v_mfma_f32_16x16x32_bf16 v[66:69], v[186:189], v[174:177], v[66:69]
	ds_read_b64_tr_b16 v[174:175], v123 offset:37760
	ds_read_b64_tr_b16 v[176:177], v123 offset:40000
	s_waitcnt lgkmcnt(6)
	v_mfma_f32_16x16x32_bf16 v[62:65], v[186:189], v[178:181], v[62:65]
	ds_read_b64_tr_b16 v[178:179], v123 offset:37792
	ds_read_b64_tr_b16 v[180:181], v123 offset:40032
	s_waitcnt lgkmcnt(6)
	v_mfma_f32_16x16x32_bf16 v[58:61], v[186:189], v[182:185], v[58:61]
	ds_read_b64_tr_b16 v[182:183], v123 offset:37824
	ds_read_b64_tr_b16 v[184:185], v123 offset:40064
	s_waitcnt lgkmcnt(6)
	v_mfma_f32_16x16x32_bf16 v[54:57], v[186:189], v[170:173], v[54:57]
	ds_read_b64_tr_b16 v[170:171], v123 offset:37856
	ds_read_b64_tr_b16 v[172:173], v123 offset:40096
	s_waitcnt lgkmcnt(6)
	v_mfma_f32_16x16x32_bf16 v[46:49], v[186:189], v[174:177], v[46:49]
	ds_read_b64_tr_b16 v[174:175], v123 offset:37888
	ds_read_b64_tr_b16 v[176:177], v123 offset:40128
	s_waitcnt lgkmcnt(6)
	v_mfma_f32_16x16x32_bf16 v[42:45], v[186:189], v[178:181], v[42:45]
	s_waitcnt lgkmcnt(4)
	v_mfma_f32_16x16x32_bf16 v[38:41], v[186:189], v[182:185], v[38:41]
	s_waitcnt lgkmcnt(2)
	v_mfma_f32_16x16x32_bf16 v[34:37], v[186:189], v[170:173], v[34:37]
	s_add_i32 s62, s62, 64
	s_add_i32 s64, s64, 1
	v_add_u32_e32 v168, 0x100, v168
	s_cmp_eq_u32 s40, s62
	s_waitcnt lgkmcnt(0)
	v_mfma_f32_16x16x32_bf16 v[50:53], v[186:189], v[174:177], v[50:53]
	v_add_u32_e32 v167, 0x100, v167
	s_cbranch_scc1 .LBB0_424
